# S5 up-projection epilogue: gate load issued before the preceding store (fresh registers), waits cover the load only (vmcnt(1))
# speedup vs baseline: 1.0053x; 1.0053x over previous
.LBB0_1300:
	v_lshl_add_u32 v148, s18, 8, v1
	s_lshl_b32 s18, s19, 8
	v_ashrrev_i32_e32 v149, 31, v148
	s_ashr_i32 s19, s18, 31
	v_lshlrev_b64 v[154:155], 11, v[148:149]
	v_lshl_add_u64 v[154:155], v[154:155], 0, s[18:19]
	v_readlane_b32 s64, v237, 61
	v_or_b32_e32 v154, v154, v138
	v_readlane_b32 s68, v238, 1
	v_readlane_b32 s69, v238, 2
	v_lshlrev_b64 v[158:159], 1, v[154:155]
	v_readlane_b32 s70, v238, 3
	v_readlane_b32 s71, v238, 4
	s_mov_b64 s[20:21], s[68:69]
	v_lshl_add_u64 v[160:161], s[20:21], 0, v[158:159]
	global_load_dwordx4 v[154:157], v[160:161], off
	v_lshl_add_u64 v[158:159], s[62:63], 0, v[158:159]
	s_andn2_b64 vcc, exec, s[0:1]
	s_mov_b64 s[0:1], -1
	v_readlane_b32 s65, v237, 62
	v_readlane_b32 s66, v237, 63
	v_readlane_b32 s67, v238, 0
	v_readlane_b32 s72, v238, 5
	v_readlane_b32 s73, v238, 6
	v_readlane_b32 s74, v238, 7
	v_readlane_b32 s75, v238, 8
	v_readlane_b32 s76, v238, 9
	v_readlane_b32 s77, v238, 10
	v_readlane_b32 s78, v238, 11
	v_readlane_b32 s79, v238, 12
	s_mov_b64 s[22:23], s[70:71]
	s_waitcnt vmcnt(0)
	v_lshlrev_b32_e32 v162, 16, v154
	v_and_b32_e32 v163, 0xffff0000, v154
	v_lshlrev_b32_e32 v154, 16, v155
	v_and_b32_e32 v155, 0xffff0000, v155
	v_lshlrev_b32_e32 v164, 16, v156
	v_and_b32_e32 v165, 0xffff0000, v156
	v_lshlrev_b32_e32 v156, 16, v157
	v_and_b32_e32 v157, 0xffff0000, v157
	v_pk_mul_f32 v[128:129], v[128:129], v[154:155]
	v_pk_mul_f32 v[154:155], v[124:125], v[156:157]
	v_pk_mul_f32 v[124:125], v[122:123], v[164:165]
	v_pk_mul_f32 v[126:127], v[126:127], v[162:163]
	s_nop 0
	v_cvt_pk_bf16_f32 v122, v126, v127
	v_cvt_pk_bf16_f32 v123, v128, v129
	v_cvt_pk_bf16_f32 v124, v124, v125
	v_cvt_pk_bf16_f32 v125, v154, v155
	global_load_dwordx4 v[200:203], v[160:161], off offset:256
	global_store_dwordx4 v[158:159], v[122:125], off
	v_or_b32_e32 v126, 16, v148
	v_ashrrev_i32_e32 v127, 31, v126
	v_lshlrev_b64 v[126:127], 11, v[126:127]
	v_lshl_add_u64 v[126:127], v[126:127], 0, s[18:19]
	v_or_b32_e32 v126, v126, v138
	v_lshlrev_b64 v[126:127], 1, v[126:127]
	v_lshl_add_u64 v[128:129], s[20:21], 0, v[126:127]
	s_waitcnt vmcnt(1)
	v_lshlrev_b32_e32 v154, 16, v200
	v_and_b32_e32 v155, 0xffff0000, v200
	v_lshlrev_b32_e32 v122, 16, v201
	v_and_b32_e32 v123, 0xffff0000, v201
	v_lshlrev_b32_e32 v156, 16, v202
	v_and_b32_e32 v157, 0xffff0000, v202
	v_lshlrev_b32_e32 v124, 16, v203
	v_and_b32_e32 v125, 0xffff0000, v203
	v_pk_mul_f32 v[120:121], v[120:121], v[122:123]
	v_pk_mul_f32 v[122:123], v[116:117], v[124:125]
	v_pk_mul_f32 v[116:117], v[114:115], v[156:157]
	v_pk_mul_f32 v[118:119], v[118:119], v[154:155]
	s_nop 0
	v_cvt_pk_bf16_f32 v114, v118, v119
	v_cvt_pk_bf16_f32 v115, v120, v121
	v_cvt_pk_bf16_f32 v116, v116, v117
	v_cvt_pk_bf16_f32 v117, v122, v123
	global_load_dwordx4 v[204:207], v[128:129], off
	global_store_dwordx4 v[158:159], v[114:117], off offset:256
	v_lshl_add_u64 v[118:119], s[62:63], 0, v[126:127]
	s_waitcnt vmcnt(1)
	v_lshlrev_b32_e32 v120, 16, v204
	v_and_b32_e32 v121, 0xffff0000, v204
	v_lshlrev_b32_e32 v114, 16, v205
	v_and_b32_e32 v115, 0xffff0000, v205
	v_lshlrev_b32_e32 v122, 16, v206
	v_and_b32_e32 v123, 0xffff0000, v206
	v_lshlrev_b32_e32 v116, 16, v207
	v_and_b32_e32 v117, 0xffff0000, v207
	v_pk_mul_f32 v[112:113], v[112:113], v[114:115]
	v_pk_mul_f32 v[114:115], v[108:109], v[116:117]
	v_pk_mul_f32 v[108:109], v[106:107], v[122:123]
	v_pk_mul_f32 v[110:111], v[110:111], v[120:121]
	s_nop 0
	v_cvt_pk_bf16_f32 v106, v110, v111
	v_cvt_pk_bf16_f32 v107, v112, v113
	v_cvt_pk_bf16_f32 v108, v108, v109
	v_cvt_pk_bf16_f32 v109, v114, v115
	global_load_dwordx4 v[200:203], v[128:129], off offset:256
	global_store_dwordx4 v[118:119], v[106:109], off
	v_or_b32_e32 v110, 32, v148
	v_ashrrev_i32_e32 v111, 31, v110
	v_lshlrev_b64 v[110:111], 11, v[110:111]
	v_lshl_add_u64 v[110:111], v[110:111], 0, s[18:19]
	v_or_b32_e32 v110, v110, v138
	v_lshlrev_b64 v[110:111], 1, v[110:111]
	v_lshl_add_u64 v[112:113], s[20:21], 0, v[110:111]
	s_waitcnt vmcnt(1)
	v_lshlrev_b32_e32 v114, 16, v200
	v_and_b32_e32 v115, 0xffff0000, v200
	v_lshlrev_b32_e32 v106, 16, v201
	v_and_b32_e32 v107, 0xffff0000, v201
	v_lshlrev_b32_e32 v116, 16, v202
	v_and_b32_e32 v117, 0xffff0000, v202
	v_lshlrev_b32_e32 v108, 16, v203
	v_and_b32_e32 v109, 0xffff0000, v203
	v_pk_mul_f32 v[104:105], v[104:105], v[106:107]
	v_pk_mul_f32 v[106:107], v[100:101], v[108:109]
	v_pk_mul_f32 v[100:101], v[98:99], v[116:117]
	v_pk_mul_f32 v[102:103], v[102:103], v[114:115]
	s_nop 0
	v_cvt_pk_bf16_f32 v98, v102, v103
	v_cvt_pk_bf16_f32 v99, v104, v105
	v_cvt_pk_bf16_f32 v100, v100, v101
	v_cvt_pk_bf16_f32 v101, v106, v107
	global_load_dwordx4 v[204:207], v[112:113], off
	global_store_dwordx4 v[118:119], v[98:101], off offset:256
	v_lshl_add_u64 v[102:103], s[62:63], 0, v[110:111]
	s_waitcnt vmcnt(1)
	v_lshlrev_b32_e32 v104, 16, v204
	v_and_b32_e32 v105, 0xffff0000, v204
	v_lshlrev_b32_e32 v98, 16, v205
	v_and_b32_e32 v99, 0xffff0000, v205
	v_lshlrev_b32_e32 v106, 16, v206
	v_and_b32_e32 v107, 0xffff0000, v206
	v_lshlrev_b32_e32 v100, 16, v207
	v_and_b32_e32 v101, 0xffff0000, v207
	v_pk_mul_f32 v[96:97], v[96:97], v[98:99]
	v_pk_mul_f32 v[98:99], v[92:93], v[100:101]
	v_pk_mul_f32 v[92:93], v[90:91], v[106:107]
	v_pk_mul_f32 v[94:95], v[94:95], v[104:105]
	s_nop 0
	v_cvt_pk_bf16_f32 v90, v94, v95
	v_cvt_pk_bf16_f32 v91, v96, v97
	v_cvt_pk_bf16_f32 v92, v92, v93
	v_cvt_pk_bf16_f32 v93, v98, v99
	global_load_dwordx4 v[200:203], v[112:113], off offset:256
	global_store_dwordx4 v[102:103], v[90:93], off
	v_or_b32_e32 v94, 48, v148
	v_ashrrev_i32_e32 v95, 31, v94
	v_lshlrev_b64 v[94:95], 11, v[94:95]
	v_lshl_add_u64 v[94:95], v[94:95], 0, s[18:19]
	v_or_b32_e32 v94, v94, v138
	v_lshlrev_b64 v[94:95], 1, v[94:95]
	v_lshl_add_u64 v[96:97], s[20:21], 0, v[94:95]
	s_waitcnt vmcnt(1)
	v_lshlrev_b32_e32 v98, 16, v200
	v_and_b32_e32 v99, 0xffff0000, v200
	v_lshlrev_b32_e32 v90, 16, v201
	v_and_b32_e32 v91, 0xffff0000, v201
	v_lshlrev_b32_e32 v100, 16, v202
	v_and_b32_e32 v101, 0xffff0000, v202
	v_lshlrev_b32_e32 v92, 16, v203
	v_and_b32_e32 v93, 0xffff0000, v203
	v_pk_mul_f32 v[88:89], v[88:89], v[90:91]
	v_pk_mul_f32 v[90:91], v[84:85], v[92:93]
	v_pk_mul_f32 v[84:85], v[82:83], v[100:101]
	v_pk_mul_f32 v[86:87], v[86:87], v[98:99]
	s_nop 0
	v_cvt_pk_bf16_f32 v82, v86, v87
	v_cvt_pk_bf16_f32 v83, v88, v89
	v_cvt_pk_bf16_f32 v84, v84, v85
	v_cvt_pk_bf16_f32 v85, v90, v91
	global_load_dwordx4 v[204:207], v[96:97], off
	global_store_dwordx4 v[102:103], v[82:85], off offset:256
	v_lshl_add_u64 v[86:87], s[62:63], 0, v[94:95]
	s_waitcnt vmcnt(1)
	v_lshlrev_b32_e32 v88, 16, v204
	v_and_b32_e32 v89, 0xffff0000, v204
	v_lshlrev_b32_e32 v82, 16, v205
	v_and_b32_e32 v83, 0xffff0000, v205
	v_lshlrev_b32_e32 v90, 16, v206
	v_and_b32_e32 v91, 0xffff0000, v206
	v_lshlrev_b32_e32 v84, 16, v207
	v_and_b32_e32 v85, 0xffff0000, v207
	v_pk_mul_f32 v[80:81], v[80:81], v[82:83]
	v_pk_mul_f32 v[82:83], v[76:77], v[84:85]
	v_pk_mul_f32 v[76:77], v[74:75], v[90:91]
	v_pk_mul_f32 v[78:79], v[78:79], v[88:89]
	s_nop 0
	v_cvt_pk_bf16_f32 v74, v78, v79
	v_cvt_pk_bf16_f32 v75, v80, v81
	v_cvt_pk_bf16_f32 v76, v76, v77
	v_cvt_pk_bf16_f32 v77, v82, v83
	global_load_dwordx4 v[200:203], v[96:97], off offset:256
	global_store_dwordx4 v[86:87], v[74:77], off
	v_add_u32_e32 v78, 0x80, v148
	v_ashrrev_i32_e32 v79, 31, v78
	v_lshlrev_b64 v[78:79], 11, v[78:79]
	v_lshl_add_u64 v[78:79], v[78:79], 0, s[18:19]
	v_or_b32_e32 v78, v78, v138
	v_lshlrev_b64 v[78:79], 1, v[78:79]
	v_lshl_add_u64 v[80:81], s[20:21], 0, v[78:79]
	s_waitcnt vmcnt(1)
	v_lshlrev_b32_e32 v82, 16, v200
	v_and_b32_e32 v83, 0xffff0000, v200
	v_lshlrev_b32_e32 v74, 16, v201
	v_and_b32_e32 v75, 0xffff0000, v201
	v_lshlrev_b32_e32 v84, 16, v202
	v_and_b32_e32 v85, 0xffff0000, v202
	v_lshlrev_b32_e32 v76, 16, v203
	v_and_b32_e32 v77, 0xffff0000, v203
	v_pk_mul_f32 v[72:73], v[72:73], v[74:75]
	v_pk_mul_f32 v[74:75], v[68:69], v[76:77]
	v_pk_mul_f32 v[68:69], v[66:67], v[84:85]
	v_pk_mul_f32 v[70:71], v[70:71], v[82:83]
	s_nop 0
	v_cvt_pk_bf16_f32 v66, v70, v71
	v_cvt_pk_bf16_f32 v67, v72, v73
	v_cvt_pk_bf16_f32 v68, v68, v69
	v_cvt_pk_bf16_f32 v69, v74, v75
	global_load_dwordx4 v[204:207], v[80:81], off
	global_store_dwordx4 v[86:87], v[66:69], off offset:256
	v_lshl_add_u64 v[70:71], s[62:63], 0, v[78:79]
	s_waitcnt vmcnt(1)
	v_lshlrev_b32_e32 v72, 16, v204
	v_and_b32_e32 v73, 0xffff0000, v204
	v_lshlrev_b32_e32 v66, 16, v205
	v_and_b32_e32 v67, 0xffff0000, v205
	v_lshlrev_b32_e32 v74, 16, v206
	v_and_b32_e32 v75, 0xffff0000, v206
	v_lshlrev_b32_e32 v68, 16, v207
	v_and_b32_e32 v69, 0xffff0000, v207
	v_pk_mul_f32 v[64:65], v[64:65], v[66:67]
	v_pk_mul_f32 v[66:67], v[60:61], v[68:69]
	v_pk_mul_f32 v[60:61], v[58:59], v[74:75]
	v_pk_mul_f32 v[62:63], v[62:63], v[72:73]
	s_nop 0
	v_cvt_pk_bf16_f32 v58, v62, v63
	v_cvt_pk_bf16_f32 v59, v64, v65
	v_cvt_pk_bf16_f32 v60, v60, v61
	v_cvt_pk_bf16_f32 v61, v66, v67
	global_load_dwordx4 v[200:203], v[80:81], off offset:256
	global_store_dwordx4 v[70:71], v[58:61], off
	v_add_u32_e32 v62, 0x90, v148
	v_ashrrev_i32_e32 v63, 31, v62
	v_lshlrev_b64 v[62:63], 11, v[62:63]
	v_lshl_add_u64 v[62:63], v[62:63], 0, s[18:19]
	v_or_b32_e32 v62, v62, v138
	v_lshlrev_b64 v[62:63], 1, v[62:63]
	v_lshl_add_u64 v[64:65], s[20:21], 0, v[62:63]
	s_waitcnt vmcnt(1)
	v_lshlrev_b32_e32 v66, 16, v200
	v_and_b32_e32 v67, 0xffff0000, v200
	v_lshlrev_b32_e32 v58, 16, v201
	v_and_b32_e32 v59, 0xffff0000, v201
	v_lshlrev_b32_e32 v68, 16, v202
	v_and_b32_e32 v69, 0xffff0000, v202
	v_lshlrev_b32_e32 v60, 16, v203
	v_and_b32_e32 v61, 0xffff0000, v203
	v_pk_mul_f32 v[56:57], v[56:57], v[58:59]
	v_pk_mul_f32 v[58:59], v[52:53], v[60:61]
	v_pk_mul_f32 v[52:53], v[50:51], v[68:69]
	v_pk_mul_f32 v[54:55], v[54:55], v[66:67]
	s_nop 0
	v_cvt_pk_bf16_f32 v50, v54, v55
	v_cvt_pk_bf16_f32 v51, v56, v57
	v_cvt_pk_bf16_f32 v52, v52, v53
	v_cvt_pk_bf16_f32 v53, v58, v59
	global_load_dwordx4 v[204:207], v[64:65], off
	global_store_dwordx4 v[70:71], v[50:53], off offset:256
	v_lshl_add_u64 v[54:55], s[62:63], 0, v[62:63]
	s_waitcnt vmcnt(1)
	v_lshlrev_b32_e32 v56, 16, v204
	v_and_b32_e32 v57, 0xffff0000, v204
	v_lshlrev_b32_e32 v50, 16, v205
	v_and_b32_e32 v51, 0xffff0000, v205
	v_lshlrev_b32_e32 v58, 16, v206
	v_and_b32_e32 v59, 0xffff0000, v206
	v_lshlrev_b32_e32 v52, 16, v207
	v_and_b32_e32 v53, 0xffff0000, v207
	v_pk_mul_f32 v[48:49], v[48:49], v[50:51]
	v_pk_mul_f32 v[50:51], v[44:45], v[52:53]
	v_pk_mul_f32 v[44:45], v[42:43], v[58:59]
	v_pk_mul_f32 v[46:47], v[46:47], v[56:57]
	s_nop 0
	v_cvt_pk_bf16_f32 v42, v46, v47
	v_cvt_pk_bf16_f32 v43, v48, v49
	v_cvt_pk_bf16_f32 v44, v44, v45
	v_cvt_pk_bf16_f32 v45, v50, v51
	global_load_dwordx4 v[200:203], v[64:65], off offset:256
	global_store_dwordx4 v[54:55], v[42:45], off
	v_add_u32_e32 v46, 0xa0, v148
	v_ashrrev_i32_e32 v47, 31, v46
	v_lshlrev_b64 v[46:47], 11, v[46:47]
	v_lshl_add_u64 v[46:47], v[46:47], 0, s[18:19]
	v_or_b32_e32 v46, v46, v138
	v_lshlrev_b64 v[46:47], 1, v[46:47]
	v_lshl_add_u64 v[48:49], s[20:21], 0, v[46:47]
	s_waitcnt vmcnt(1)
	v_lshlrev_b32_e32 v50, 16, v200
	v_and_b32_e32 v51, 0xffff0000, v200
	v_lshlrev_b32_e32 v42, 16, v201
	v_and_b32_e32 v43, 0xffff0000, v201
	v_lshlrev_b32_e32 v52, 16, v202
	v_and_b32_e32 v53, 0xffff0000, v202
	v_lshlrev_b32_e32 v44, 16, v203
	v_and_b32_e32 v45, 0xffff0000, v203
	v_pk_mul_f32 v[40:41], v[40:41], v[42:43]
	v_pk_mul_f32 v[42:43], v[36:37], v[44:45]
	v_pk_mul_f32 v[36:37], v[34:35], v[52:53]
	v_pk_mul_f32 v[38:39], v[38:39], v[50:51]
	s_nop 0
	v_cvt_pk_bf16_f32 v34, v38, v39
	v_cvt_pk_bf16_f32 v35, v40, v41
	v_cvt_pk_bf16_f32 v36, v36, v37
	v_cvt_pk_bf16_f32 v37, v42, v43
	global_load_dwordx4 v[204:207], v[48:49], off
	global_store_dwordx4 v[54:55], v[34:37], off offset:256
	v_lshl_add_u64 v[38:39], s[62:63], 0, v[46:47]
	s_waitcnt vmcnt(1)
	v_lshlrev_b32_e32 v40, 16, v204
	v_and_b32_e32 v41, 0xffff0000, v204
	v_lshlrev_b32_e32 v34, 16, v205
	v_and_b32_e32 v35, 0xffff0000, v205
	v_lshlrev_b32_e32 v42, 16, v206
	v_and_b32_e32 v43, 0xffff0000, v206
	v_lshlrev_b32_e32 v36, 16, v207
	v_and_b32_e32 v37, 0xffff0000, v207
	v_pk_mul_f32 v[32:33], v[32:33], v[34:35]
	v_pk_mul_f32 v[34:35], v[28:29], v[36:37]
	v_pk_mul_f32 v[28:29], v[26:27], v[42:43]
	v_pk_mul_f32 v[30:31], v[30:31], v[40:41]
	s_nop 0
	v_cvt_pk_bf16_f32 v26, v30, v31
	v_cvt_pk_bf16_f32 v27, v32, v33
	v_cvt_pk_bf16_f32 v28, v28, v29
	v_cvt_pk_bf16_f32 v29, v34, v35
	global_load_dwordx4 v[200:203], v[48:49], off offset:256
	global_store_dwordx4 v[38:39], v[26:29], off
	v_add_u32_e32 v30, 0xb0, v148
	v_ashrrev_i32_e32 v31, 31, v30
	v_lshlrev_b64 v[30:31], 11, v[30:31]
	v_lshl_add_u64 v[30:31], v[30:31], 0, s[18:19]
	v_or_b32_e32 v30, v30, v138
	v_lshlrev_b64 v[30:31], 1, v[30:31]
	v_lshl_add_u64 v[32:33], s[20:21], 0, v[30:31]
	s_waitcnt vmcnt(1)
	v_lshlrev_b32_e32 v34, 16, v200
	v_and_b32_e32 v35, 0xffff0000, v200
	v_lshlrev_b32_e32 v26, 16, v201
	v_and_b32_e32 v27, 0xffff0000, v201
	v_lshlrev_b32_e32 v36, 16, v202
	v_and_b32_e32 v37, 0xffff0000, v202
	v_lshlrev_b32_e32 v28, 16, v203
	v_and_b32_e32 v29, 0xffff0000, v203
	v_pk_mul_f32 v[24:25], v[24:25], v[26:27]
	v_pk_mul_f32 v[26:27], v[20:21], v[28:29]
	v_pk_mul_f32 v[20:21], v[18:19], v[36:37]
	v_pk_mul_f32 v[22:23], v[22:23], v[34:35]
	s_nop 0
	v_cvt_pk_bf16_f32 v18, v22, v23
	v_cvt_pk_bf16_f32 v19, v24, v25
	v_cvt_pk_bf16_f32 v20, v20, v21
	v_cvt_pk_bf16_f32 v21, v26, v27
	global_load_dwordx4 v[204:207], v[32:33], off
	global_store_dwordx4 v[38:39], v[18:21], off offset:256
	v_lshl_add_u64 v[22:23], s[62:63], 0, v[30:31]
	s_waitcnt vmcnt(1)
	v_lshlrev_b32_e32 v24, 16, v204
	v_and_b32_e32 v25, 0xffff0000, v204
	v_lshlrev_b32_e32 v18, 16, v205
	v_and_b32_e32 v19, 0xffff0000, v205
	v_lshlrev_b32_e32 v26, 16, v206
	v_and_b32_e32 v27, 0xffff0000, v206
	v_lshlrev_b32_e32 v20, 16, v207
	v_and_b32_e32 v21, 0xffff0000, v207
	v_pk_mul_f32 v[16:17], v[16:17], v[18:19]
	v_pk_mul_f32 v[18:19], v[12:13], v[20:21]
	v_pk_mul_f32 v[12:13], v[10:11], v[26:27]
	v_pk_mul_f32 v[14:15], v[14:15], v[24:25]
	s_nop 0
	v_cvt_pk_bf16_f32 v10, v14, v15
	v_cvt_pk_bf16_f32 v11, v16, v17
	v_cvt_pk_bf16_f32 v12, v12, v13
	v_cvt_pk_bf16_f32 v13, v18, v19
	global_load_dwordx4 v[200:203], v[32:33], off offset:256
	global_store_dwordx4 v[22:23], v[10:13], off
	s_waitcnt vmcnt(1)
	v_lshlrev_b32_e32 v14, 16, v200
	v_and_b32_e32 v15, 0xffff0000, v200
	v_lshlrev_b32_e32 v10, 16, v201
	v_and_b32_e32 v11, 0xffff0000, v201
	v_lshlrev_b32_e32 v16, 16, v202
	v_and_b32_e32 v17, 0xffff0000, v202
	v_lshlrev_b32_e32 v12, 16, v203
	v_and_b32_e32 v13, 0xffff0000, v203
	v_pk_mul_f32 v[8:9], v[8:9], v[10:11]
	v_pk_mul_f32 v[10:11], v[4:5], v[12:13]
	v_pk_mul_f32 v[4:5], v[2:3], v[16:17]
	v_pk_mul_f32 v[6:7], v[6:7], v[14:15]
	s_nop 0
	v_cvt_pk_bf16_f32 v2, v6, v7
	v_cvt_pk_bf16_f32 v3, v8, v9
	v_cvt_pk_bf16_f32 v4, v4, v5
	v_cvt_pk_bf16_f32 v5, v10, v11
	global_store_dwordx4 v[22:23], v[2:5], off offset:256
	s_cbranch_vccnz .LBB0_1289
	s_andn2_b64 vcc, exec, s[4:5]
	s_cbranch_vccnz .LBB0_1288
	s_barrier
	s_branch .LBB0_1288
